# P6 loop top: second row's Y loads and first parameter batch issued with the first row's loads, vmcnt waits recomputed
# baseline (speedup 1.0000x reference)
.LBB0_776:
	s_lshl_b32 s8, s46, 4
	s_add_i32 s20, s8, s30
	s_lshr_b32 s8, s20, 12
	s_mulk_i32 s8, 0x3000
	s_ashr_i32 s9, s8, 31
	s_lshl_b64 s[8:9], s[8:9], 2
	s_add_u32 s28, s31, s8
	s_addc_u32 s29, s33, s9
	s_add_u32 s22, s28, 0x6000
	s_addc_u32 s23, s29, 0
	s_ashr_i32 s21, s20, 31
	s_lshl_b64 s[24:25], s[20:21], 12
	v_lshl_add_u64 v[2:3], v[44:45], 0, s[24:25]
	global_load_dwordx2 v[4:5], v[2:3], off offset:1536
	global_load_dwordx2 v[6:7], v[2:3], off offset:2048
	global_load_dwordx2 v[8:9], v[2:3], off offset:3072
	global_load_dwordx2 v[10:11], v[2:3], off offset:3584
	global_load_dwordx2 v[12:13], v[2:3], off offset:512
	global_load_dwordx2 v[16:17], v[2:3], off
	global_load_dwordx2 v[36:37], v[2:3], off offset:1024
	global_load_dwordx2 v[38:39], v[2:3], off offset:2560
	s_or_b32 s8, s20, 1
	s_ashr_i32 s9, s8, 31
	s_lshl_b64 s[26:27], s[8:9], 12
	v_lshl_add_u64 v[100:101], v[44:45], 0, s[26:27]
	global_load_dwordx2 v[102:103], v[100:101], off offset:1536
	s_add_u32 s28, s28, 0x8000
	s_addc_u32 s29, s29, 0
	v_lshl_add_u64 v[210:211], v[64:65], 0, s[24:25]
	global_load_dwordx2 v[242:243], v[100:101], off
	global_load_dwordx2 v[40:41], v[100:101], off offset:512
	global_load_dwordx2 v[120:121], v[100:101], off offset:1024
	global_load_dwordx2 v[106:107], v[100:101], off offset:2048
	global_load_dwordx2 v[244:245], v[100:101], off offset:2560
	global_load_dwordx2 v[122:123], v[100:101], off offset:3072
	global_load_dwordx2 v[100:101], v[100:101], off offset:3584
	v_lshlrev_b32_e32 v246, 2, v58
	v_lshlrev_b32_e32 v247, 2, v60
	v_lshlrev_b32_e32 v248, 2, v62
	global_load_dwordx4 v[156:159], v[54:55], off offset:1024
	global_load_dwordx4 v[160:163], v[56:57], off offset:1024
	global_load_dwordx4 v[164:167], v[56:57], off offset:2048
	global_load_dwordx4 v[168:171], v[54:55], off offset:3072
	global_load_dwordx4 v[172:175], v[56:57], off offset:3072
	global_load_dwordx4 v[176:179], v150, s[22:23]
	global_load_dwordx4 v[180:183], v246, s[28:29]
	global_load_dwordx4 v[184:187], v246, s[22:23]
	global_load_dwordx4 v[188:191], v247, s[28:29]
	global_load_dwordx4 v[192:195], v247, s[22:23]
	global_load_dwordx4 v[196:199], v248, s[28:29]
	global_load_dwordx4 v[200:203], v248, s[22:23]
	s_waitcnt vmcnt(19)
	v_lshlrev_b32_e32 v2, 16, v4
	v_lshlrev_b32_e32 v25, 16, v6
	v_and_b32_e32 v21, 0xffff0000, v6
	v_lshlrev_b32_e32 v23, 16, v7
	v_lshlrev_b32_e32 v35, 16, v12
	v_lshlrev_b32_e32 v34, 16, v16
	v_and_b32_e32 v33, 0xffff0000, v12
	v_and_b32_e32 v32, 0xffff0000, v16
	v_lshlrev_b32_e32 v31, 16, v13
	v_lshlrev_b32_e32 v30, 16, v17
	v_and_b32_e32 v15, 0xffff0000, v13
	v_and_b32_e32 v14, 0xffff0000, v17
	v_and_b32_e32 v19, 0xffff0000, v7
	v_lshlrev_b32_e32 v26, 16, v8
	v_and_b32_e32 v27, 0xffff0000, v8
	v_lshlrev_b32_e32 v28, 16, v9
	v_and_b32_e32 v29, 0xffff0000, v9
	v_lshlrev_b32_e32 v94, 16, v10
	v_and_b32_e32 v95, 0xffff0000, v10
	v_lshlrev_b32_e32 v97, 16, v11
	v_and_b32_e32 v93, 0xffff0000, v11
	v_lshlrev_b32_e32 v7, 16, v37
	v_lshlrev_b32_e32 v6, 16, v36
	v_and_b32_e32 v105, 0xffff0000, v37
	v_and_b32_e32 v104, 0xffff0000, v36
	v_pk_add_f32 v[8:9], v[34:35], v[32:33]
	v_pk_add_f32 v[10:11], v[30:31], v[14:15]
	v_pk_add_f32 v[12:13], v[6:7], v[104:105]
	v_pk_add_f32 v[8:9], v[8:9], v[10:11]
	v_and_b32_e32 v3, 0xffff0000, v4
	v_lshlrev_b32_e32 v4, 16, v5
	v_and_b32_e32 v5, 0xffff0000, v5
	v_pk_add_f32 v[10:11], v[12:13], v[12:13] op_sel:[0,1] op_sel_hi:[1,0]
	v_add_f32_e32 v8, 0, v8
	v_add_f32_e32 v22, v2, v3
	v_add_f32_e32 v18, v4, v5
	v_mov_b32_e32 v11, v21
	v_add_f32_e32 v24, v8, v9
	v_lshlrev_b32_e32 v99, 16, v39
	v_lshlrev_b32_e32 v98, 16, v38
	v_and_b32_e32 v39, 0xffff0000, v39
	v_and_b32_e32 v38, 0xffff0000, v38
	v_pk_add_f32 v[12:13], v[22:23], v[18:19]
	v_pk_add_f32 v[8:9], v[24:25], v[10:11]
	v_pk_add_f32 v[16:17], v[98:99], v[38:39]
	v_pk_add_f32 v[8:9], v[8:9], v[12:13]
	v_pk_add_f32 v[16:17], v[16:17], v[16:17] op_sel:[0,1] op_sel_hi:[1,0]
	v_pk_add_f32 v[8:9], v[8:9], v[8:9] op_sel:[0,1] op_sel_hi:[1,0]
	v_add_f32_e32 v96, v26, v27
	v_add_f32_e32 v92, v28, v29
	v_mov_b32_e32 v17, v95
	v_mov_b32_e32 v9, v94
	v_pk_add_f32 v[36:37], v[96:97], v[92:93]
	v_pk_add_f32 v[8:9], v[8:9], v[16:17]
	v_pk_add_f32 v[8:9], v[8:9], v[36:37]
	s_nop 0
	v_add_f32_e32 v8, v8, v9
	ds_bpermute_b32 v9, v1, v8
	v_lshlrev_b32_e32 v10, 16, v103
	v_and_b32_e32 v11, 0xffff0000, v103
	s_waitcnt lgkmcnt(0)
	v_add_f32_e32 v8, v8, v9
	ds_bpermute_b32 v9, v49, v8
	s_waitcnt lgkmcnt(0)
	v_add_f32_e32 v8, v8, v9
	ds_bpermute_b32 v9, v59, v8
	s_waitcnt lgkmcnt(0)
	v_add_f32_e32 v8, v8, v9
	ds_bpermute_b32 v9, v61, v8
	s_waitcnt lgkmcnt(0)
	v_add_f32_e32 v8, v8, v9
	ds_bpermute_b32 v9, v63, v8
	s_waitcnt lgkmcnt(0)
	v_add_f32_e32 v12, v8, v9
	ds_bpermute_b32 v13, v67, v12
	v_lshlrev_b32_e32 v8, 16, v102
	v_and_b32_e32 v9, 0xffff0000, v102
	v_add_f32_e32 v116, v8, v9
	s_waitcnt lgkmcnt(0)
	v_add_f32_e32 v22, v12, v13
	v_fmac_f32_e32 v14, 0xba000000, v22
	v_fmac_f32_e32 v32, 0xba000000, v22
	v_fmac_f32_e32 v15, 0xba000000, v22
	v_fmac_f32_e32 v33, 0xba000000, v22
	v_fmac_f32_e32 v104, 0xba000000, v22
	v_fmac_f32_e32 v105, 0xba000000, v22
	v_fmac_f32_e32 v7, 0xba000000, v22
	v_fmac_f32_e32 v30, 0xba000000, v22
	v_fmac_f32_e32 v34, 0xba000000, v22
	v_fmac_f32_e32 v31, 0xba000000, v22
	v_fmac_f32_e32 v35, 0xba000000, v22
	v_fmac_f32_e32 v6, 0xba000000, v22
	v_pk_mul_f32 v[102:103], v[32:33], v[32:33]
	v_pk_mul_f32 v[108:109], v[14:15], v[14:15]
	v_mov_b32_e32 v12, v7
	v_mov_b32_e32 v13, v105
	v_mov_b32_e32 v7, v104
	v_pk_fma_f32 v[102:103], v[34:35], v[34:35], v[102:103]
	v_pk_fma_f32 v[104:105], v[30:31], v[30:31], v[108:109]
	v_pk_mul_f32 v[108:109], v[12:13], v[12:13]
	v_pk_mul_f32 v[110:111], v[6:7], v[6:7]
	v_fmac_f32_e32 v2, 0xba000000, v22
	v_fmac_f32_e32 v4, 0xba000000, v22
	v_pk_add_f32 v[102:103], v[102:103], v[104:105]
	v_pk_mov_b32 v[104:105], v[110:111], v[108:109] op_sel:[1,0]
	v_mov_b32_e32 v111, v109
	v_fmac_f32_e32 v3, 0xba000000, v22
	v_fmac_f32_e32 v5, 0xba000000, v22
	v_fmac_f32_e32 v19, 0xba000000, v22
	v_fmac_f32_e32 v21, 0xba000000, v22
	v_mul_f32_e32 v18, v2, v2
	v_mul_f32_e32 v20, v4, v4
	v_pk_add_f32 v[104:105], v[104:105], v[110:111]
	v_fmac_f32_e32 v23, 0xba000000, v22
	v_fmac_f32_e32 v25, 0xba000000, v22
	v_pk_fma_f32 v[112:113], v[2:3], v[2:3], v[18:19] op_sel_hi:[1,1,0]
	v_pk_fma_f32 v[114:115], v[4:5], v[4:5], v[20:21] op_sel_hi:[1,1,0]
	v_pk_add_f32 v[102:103], v[102:103], v[102:103] op_sel_hi:[0,1]
	v_pk_add_f32 v[104:105], v[104:105], v[104:105] op_sel_hi:[0,1]
	v_fmac_f32_e32 v38, 0xba000000, v22
	v_fmac_f32_e32 v39, 0xba000000, v22
	v_fmac_f32_e32 v99, 0xba000000, v22
	v_mul_f32_e32 v112, v25, v25
	v_mul_f32_e32 v114, v21, v21
	v_mul_f32_e32 v104, v23, v23
	v_mul_f32_e32 v102, v19, v19
	v_fmac_f32_e32 v98, 0xba000000, v22
	v_mov_b32_e32 v110, v99
	v_mov_b32_e32 v111, v39
	v_mov_b32_e32 v99, v38
	v_pk_add_f32 v[108:109], v[112:113], v[114:115]
	v_pk_add_f32 v[102:103], v[104:105], v[102:103]
	v_pk_mul_f32 v[104:105], v[110:111], v[110:111]
	v_pk_mul_f32 v[38:39], v[98:99], v[98:99]
	v_fmac_f32_e32 v26, 0xba000000, v22
	v_pk_add_f32 v[102:103], v[108:109], v[102:103]
	v_pk_mov_b32 v[108:109], v[38:39], v[104:105] op_sel:[1,0]
	v_mov_b32_e32 v39, v105
	v_fmac_f32_e32 v27, 0xba000000, v22
	v_fmac_f32_e32 v28, 0xba000000, v22
	v_mul_f32_e32 v18, v26, v26
	v_pk_add_f32 v[38:39], v[108:109], v[38:39]
	v_fmac_f32_e32 v29, 0xba000000, v22
	v_pk_fma_f32 v[104:105], v[26:27], v[26:27], v[18:19] op_sel_hi:[1,1,0]
	v_mul_f32_e32 v18, v28, v28
	v_pk_add_f32 v[102:103], v[102:103], v[102:103] op_sel_hi:[0,1]
	v_pk_add_f32 v[38:39], v[38:39], v[38:39] op_sel_hi:[0,1]
	v_pk_fma_f32 v[108:109], v[28:29], v[28:29], v[18:19] op_sel_hi:[1,1,0]
	v_fmac_f32_e32 v93, 0xba000000, v22
	v_fmac_f32_e32 v97, 0xba000000, v22
	v_fmac_f32_e32 v95, 0xba000000, v22
	v_fmac_f32_e32 v94, 0xba000000, v22
	v_mul_f32_e32 v104, v94, v94
	v_mul_f32_e32 v108, v95, v95
	v_mul_f32_e32 v38, v97, v97
	v_mul_f32_e32 v102, v93, v93
	v_pk_add_f32 v[104:105], v[104:105], v[108:109]
	v_pk_add_f32 v[38:39], v[38:39], v[102:103]
	s_waitcnt vmcnt(17)
	v_mov_b32_e32 v16, v242
	v_mov_b32_e32 v17, v243
	v_lshlrev_b32_e32 v125, 16, v40
	v_pk_add_f32 v[38:39], v[104:105], v[38:39]
	v_lshlrev_b32_e32 v124, 16, v16
	v_add_f32_e32 v18, v38, v39
	ds_bpermute_b32 v20, v1, v18
	v_and_b32_e32 v127, 0xffff0000, v40
	v_and_b32_e32 v126, 0xffff0000, v16
	v_lshlrev_b32_e32 v39, 16, v41
	v_lshlrev_b32_e32 v38, 16, v17
	v_and_b32_e32 v41, 0xffff0000, v41
	v_and_b32_e32 v40, 0xffff0000, v17
	s_waitcnt vmcnt(15)
	v_lshlrev_b32_e32 v119, 16, v106
	v_and_b32_e32 v115, 0xffff0000, v106
	v_lshlrev_b32_e32 v117, 16, v107
	v_and_b32_e32 v113, 0xffff0000, v107
	s_waitcnt vmcnt(13)
	v_mov_b32_e32 v36, v244
	v_mov_b32_e32 v37, v245
	v_lshlrev_b32_e32 v108, 16, v122
	v_and_b32_e32 v109, 0xffff0000, v122
	v_lshlrev_b32_e32 v106, 16, v123
	v_and_b32_e32 v107, 0xffff0000, v123
	v_pk_add_f32 v[16:17], v[124:125], v[126:127]
	v_pk_add_f32 v[122:123], v[38:39], v[40:41]
	s_waitcnt lgkmcnt(0)
	v_add_f32_e32 v18, v18, v20
	v_pk_add_f32 v[16:17], v[16:17], v[122:123]
	ds_bpermute_b32 v20, v49, v18
	v_add_f32_e32 v16, 0, v16
	v_add_f32_e32 v118, v16, v17
	v_lshlrev_b32_e32 v17, 16, v121
	v_lshlrev_b32_e32 v16, 16, v120
	v_and_b32_e32 v123, 0xffff0000, v121
	v_and_b32_e32 v122, 0xffff0000, v120
	v_pk_add_f32 v[120:121], v[16:17], v[122:123]
	v_add_f32_e32 v112, v10, v11
	v_pk_add_f32 v[120:121], v[120:121], v[120:121] op_sel:[0,1] op_sel_hi:[1,0]
	v_pk_add_f32 v[128:129], v[116:117], v[112:113]
	v_mov_b32_e32 v121, v115
	v_pk_add_f32 v[120:121], v[118:119], v[120:121]
	s_waitcnt lgkmcnt(0)
	v_add_f32_e32 v18, v18, v20
	v_pk_add_f32 v[128:129], v[120:121], v[128:129]
	v_lshlrev_b32_e32 v121, 16, v37
	v_lshlrev_b32_e32 v120, 16, v36
	v_and_b32_e32 v131, 0xffff0000, v37
	v_and_b32_e32 v130, 0xffff0000, v36
	ds_bpermute_b32 v20, v59, v18
	v_pk_add_f32 v[36:37], v[120:121], v[130:131]
	s_waitcnt vmcnt(12)
	v_lshlrev_b32_e32 v104, 16, v100
	v_and_b32_e32 v105, 0xffff0000, v100
	v_pk_add_f32 v[128:129], v[128:129], v[128:129] op_sel:[0,1] op_sel_hi:[1,0]
	v_pk_add_f32 v[36:37], v[36:37], v[36:37] op_sel:[0,1] op_sel_hi:[1,0]
	v_lshlrev_b32_e32 v103, 16, v101
	v_and_b32_e32 v101, 0xffff0000, v101
	v_add_f32_e32 v102, v108, v109
	v_add_f32_e32 v100, v106, v107
	v_mov_b32_e32 v129, v104
	v_mov_b32_e32 v37, v105
	v_pk_add_f32 v[36:37], v[128:129], v[36:37]
	v_pk_add_f32 v[128:129], v[102:103], v[100:101]
	s_waitcnt lgkmcnt(0)
	v_add_f32_e32 v18, v18, v20
	v_pk_add_f32 v[36:37], v[36:37], v[128:129]
	ds_bpermute_b32 v20, v61, v18
	v_add_f32_e32 v22, v36, v37
	ds_bpermute_b32 v24, v1, v22
	v_mov_b32_e32 v37, v33
	v_mov_b32_e32 v33, v15
	s_waitcnt lgkmcnt(1)
	v_add_f32_e32 v18, v18, v20
	ds_bpermute_b32 v20, v63, v18
	s_waitcnt lgkmcnt(1)
	v_add_f32_e32 v22, v22, v24
	ds_bpermute_b32 v24, v49, v22
	v_mov_b32_e32 v128, v30
	v_mov_b32_e32 v36, v35
	s_waitcnt lgkmcnt(1)
	v_add_f32_e32 v18, v18, v20
	ds_bpermute_b32 v20, v67, v18
	s_waitcnt lgkmcnt(1)
	v_add_f32_e32 v22, v22, v24
	ds_bpermute_b32 v24, v59, v22
	v_mov_b32_e32 v35, v32
	v_mov_b32_e32 v32, v31
	s_waitcnt lgkmcnt(1)
	v_add_f32_e32 v18, v18, v20
	v_fmamk_f32 v18, v18, 0x3a000000, v148
	s_waitcnt lgkmcnt(0)
	v_add_f32_e32 v20, v22, v24
	ds_bpermute_b32 v22, v61, v20
	v_mul_f32_e32 v24, 0x4f800000, v18
	v_cmp_gt_f32_e32 vcc, s36, v18
	v_mov_b32_e32 v129, v14
	v_lshlrev_b32_e32 v100, 1, v78
	s_waitcnt lgkmcnt(0)
	v_add_f32_e32 v20, v20, v22
	ds_bpermute_b32 v22, v63, v20
	v_cndmask_b32_e32 v24, v18, v24, vcc
	v_sqrt_f32_e32 v18, v24
	s_waitcnt lgkmcnt(0)
	v_add_f32_e32 v20, v20, v22
	ds_bpermute_b32 v22, v67, v20
	v_add_u32_e32 v15, -1, v18
	v_fma_f32 v30, -v15, v18, v24
	v_cmp_ge_f32_e64 s[8:9], 0, v30
	v_add_u32_e32 v42, 1, v18
	s_waitcnt lgkmcnt(0)
	v_add_f32_e32 v20, v20, v22
	v_fmac_f32_e32 v40, 0xba000000, v20
	v_fmac_f32_e32 v126, 0xba000000, v20
	v_fmac_f32_e32 v41, 0xba000000, v20
	v_fmac_f32_e32 v127, 0xba000000, v20
	v_fmac_f32_e32 v38, 0xba000000, v20
	v_fmac_f32_e32 v124, 0xba000000, v20
	v_fmac_f32_e32 v39, 0xba000000, v20
	v_fmac_f32_e32 v125, 0xba000000, v20
	v_pk_mul_f32 v[30:31], v[126:127], v[126:127]
	v_pk_mul_f32 v[132:133], v[40:41], v[40:41]
	v_pk_fma_f32 v[30:31], v[124:125], v[124:125], v[30:31]
	v_pk_fma_f32 v[132:133], v[38:39], v[38:39], v[132:133]
	v_fmac_f32_e32 v122, 0xba000000, v20
	v_pk_add_f32 v[30:31], v[30:31], v[132:133]
	v_fmac_f32_e32 v123, 0xba000000, v20
	v_fmac_f32_e32 v17, 0xba000000, v20
	v_pk_add_f32 v[132:133], v[30:31], v[30:31] op_sel_hi:[0,1]
	v_fmac_f32_e32 v16, 0xba000000, v20
	v_mov_b32_e32 v30, v17
	v_mov_b32_e32 v31, v123
	v_mov_b32_e32 v17, v122
	v_pk_mul_f32 v[134:135], v[30:31], v[30:31]
	v_pk_mul_f32 v[122:123], v[16:17], v[16:17]
	v_fmac_f32_e32 v8, 0xba000000, v20
	v_cndmask_b32_e64 v15, v18, v15, s[8:9]
	v_fma_f32 v92, -v42, v18, v24
	v_pk_mov_b32 v[136:137], v[122:123], v[134:135] op_sel:[1,0]
	v_mov_b32_e32 v123, v135
	v_fmac_f32_e32 v9, 0xba000000, v20
	v_fmac_f32_e32 v10, 0xba000000, v20
	v_mul_f32_e32 v18, v8, v8
	v_pk_add_f32 v[122:123], v[136:137], v[122:123]
	v_fmac_f32_e32 v11, 0xba000000, v20
	v_pk_fma_f32 v[134:135], v[8:9], v[8:9], v[18:19] op_sel_hi:[1,1,0]
	v_mul_f32_e32 v18, v10, v10
	v_pk_add_f32 v[122:123], v[122:123], v[122:123] op_sel_hi:[0,1]
	v_pk_fma_f32 v[136:137], v[10:11], v[10:11], v[18:19] op_sel_hi:[1,1,0]
	v_fmac_f32_e32 v113, 0xba000000, v20
	v_fmac_f32_e32 v117, 0xba000000, v20
	v_fmac_f32_e32 v115, 0xba000000, v20
	v_fmac_f32_e32 v119, 0xba000000, v20
	v_mul_f32_e32 v134, v119, v119
	v_mul_f32_e32 v136, v115, v115
	v_mul_f32_e32 v122, v117, v117
	v_mul_f32_e32 v132, v113, v113
	v_pk_add_f32 v[134:135], v[134:135], v[136:137]
	v_pk_add_f32 v[122:123], v[122:123], v[132:133]
	v_fmac_f32_e32 v130, 0xba000000, v20
	v_pk_add_f32 v[122:123], v[134:135], v[122:123]
	v_fmac_f32_e32 v131, 0xba000000, v20
	v_fmac_f32_e32 v121, 0xba000000, v20
	v_pk_add_f32 v[132:133], v[122:123], v[122:123] op_sel_hi:[0,1]
	v_fmac_f32_e32 v120, 0xba000000, v20
	v_mov_b32_e32 v122, v121
	v_mov_b32_e32 v123, v131
	v_mov_b32_e32 v121, v130
	v_pk_mul_f32 v[134:135], v[122:123], v[122:123]
	v_pk_mul_f32 v[130:131], v[120:121], v[120:121]
	v_fmac_f32_e32 v108, 0xba000000, v20
	v_pk_mov_b32 v[136:137], v[130:131], v[134:135] op_sel:[1,0]
	v_mov_b32_e32 v131, v135
	v_fmac_f32_e32 v109, 0xba000000, v20
	v_fmac_f32_e32 v106, 0xba000000, v20
	v_mul_f32_e32 v18, v108, v108
	v_pk_add_f32 v[130:131], v[136:137], v[130:131]
	v_fmac_f32_e32 v107, 0xba000000, v20
	v_pk_fma_f32 v[134:135], v[108:109], v[108:109], v[18:19] op_sel_hi:[1,1,0]
	v_mul_f32_e32 v18, v106, v106
	v_pk_add_f32 v[130:131], v[130:131], v[130:131] op_sel_hi:[0,1]
	v_pk_fma_f32 v[136:137], v[106:107], v[106:107], v[18:19] op_sel_hi:[1,1,0]
	v_fmac_f32_e32 v101, 0xba000000, v20
	v_fmac_f32_e32 v103, 0xba000000, v20
	v_fmac_f32_e32 v105, 0xba000000, v20
	v_fmac_f32_e32 v104, 0xba000000, v20
	v_mul_f32_e32 v134, v104, v104
	v_mul_f32_e32 v136, v105, v105
	v_mul_f32_e32 v130, v103, v103
	v_mul_f32_e32 v132, v101, v101
	v_pk_add_f32 v[134:135], v[134:135], v[136:137]
	v_pk_add_f32 v[130:131], v[130:131], v[132:133]
	v_cmp_lt_f32_e64 s[8:9], 0, v92
	v_pk_add_f32 v[130:131], v[134:135], v[130:131]
	v_mov_b32_e32 v138, v124
	v_add_f32_e32 v18, v130, v131
	ds_bpermute_b32 v20, v1, v18
	v_cndmask_b32_e64 v15, v15, v42, s[8:9]
	v_mul_f32_e32 v22, 0x37800000, v15
	v_cndmask_b32_e32 v15, v15, v22, vcc
	v_cmp_class_f32_e32 vcc, v24, v149
	s_waitcnt lgkmcnt(0)
	v_add_f32_e32 v18, v18, v20
	ds_bpermute_b32 v20, v49, v18
	v_cndmask_b32_e32 v15, v15, v24, vcc
	v_div_scale_f32 v22, s[8:9], v15, v15, 1.0
	v_rcp_f32_e32 v24, v22
	s_waitcnt lgkmcnt(0)
	v_add_f32_e32 v18, v18, v20
	ds_bpermute_b32 v20, v59, v18
	global_load_dwordx4 v[130:133], v[54:55], off
	global_load_dwordx4 v[134:137], v[56:57], off
	v_mov_b32_e32 v139, v126
	v_mov_b32_e32 v206, v38
	s_waitcnt lgkmcnt(0)
	v_add_f32_e32 v14, v18, v20
	ds_bpermute_b32 v18, v61, v14
	v_fma_f32 v20, -v22, v24, 1.0
	v_fmac_f32_e32 v24, v20, v24
	v_div_scale_f32 v20, vcc, 1.0, v15, 1.0
	s_waitcnt lgkmcnt(0)
	v_add_f32_e32 v14, v14, v18
	ds_bpermute_b32 v18, v63, v14
	v_mul_f32_e32 v42, v20, v24
	v_fma_f32 v92, -v22, v42, v20
	v_fmac_f32_e32 v42, v92, v24
	v_fma_f32 v20, -v22, v42, v20
	s_waitcnt lgkmcnt(0)
	v_add_f32_e32 v18, v14, v18
	ds_bpermute_b32 v22, v67, v18
	v_div_fmas_f32 v14, v20, v24, v42
	v_div_fixup_f32 v96, v14, v15, 1.0
	v_mov_b32_e32 v14, v125
	v_mov_b32_e32 v15, v127
	s_waitcnt lgkmcnt(0)
	v_add_f32_e32 v18, v18, v22
	v_fmamk_f32 v18, v18, 0x3a000000, v148
	v_mul_f32_e32 v20, 0x4f800000, v18
	v_cmp_gt_f32_e32 vcc, s36, v18
	global_load_dwordx4 v[124:127], v[54:55], off offset:2048
	v_cndmask_b32_e32 v18, v18, v20, vcc
	v_sqrt_f32_e32 v20, v18
	v_mov_b32_e32 v204, v39
	v_mov_b32_e32 v205, v41
	v_add_u32_e32 v22, -1, v20
	v_fma_f32 v24, -v22, v20, v18
	v_cmp_ge_f32_e64 s[8:9], 0, v24
	v_add_u32_e32 v24, 1, v20
	v_mov_b32_e32 v207, v40
	v_cndmask_b32_e64 v22, v20, v22, s[8:9]
	v_fma_f32 v20, -v24, v20, v18
	v_cmp_lt_f32_e64 s[8:9], 0, v20
	v_pk_mul_f32 v[34:35], v[34:35], v[96:97] op_sel_hi:[1,0]
	v_pk_mul_f32 v[128:129], v[128:129], v[96:97] op_sel_hi:[1,0]
	v_cndmask_b32_e64 v20, v22, v24, s[8:9]
	v_mul_f32_e32 v22, 0x37800000, v20
	v_cndmask_b32_e32 v20, v20, v22, vcc
	v_cmp_class_f32_e32 vcc, v18, v149
	v_pk_mul_f32 v[36:37], v[36:37], v[96:97] op_sel_hi:[1,0]
	v_pk_mul_f32 v[32:33], v[32:33], v[96:97] op_sel_hi:[1,0]
	v_cndmask_b32_e32 v18, v20, v18, vcc
	v_div_scale_f32 v20, s[8:9], v18, v18, 1.0
	v_rcp_f32_e32 v22, v20
	s_add_u32 s8, s16, s24
	s_addc_u32 s9, s17, s25
	s_add_u32 s24, s16, s26
	v_fma_f32 v24, -v20, v22, 1.0
	v_fmac_f32_e32 v22, v24, v22
	v_div_scale_f32 v24, vcc, 1.0, v18, 1.0
	v_mul_f32_e32 v38, v24, v22
	v_fma_f32 v39, -v20, v38, v24
	v_fmac_f32_e32 v38, v39, v22
	v_fma_f32 v20, -v20, v38, v24
	v_div_fmas_f32 v20, v20, v22, v38
	v_div_fixup_f32 v42, v20, v18, 1.0
	global_load_dwordx4 v[38:41], v150, s[28:29]
	v_lshlrev_b32_e32 v18, 2, v58
	v_lshlrev_b32_e32 v18, 2, v60
	v_pk_mul_f32 v[138:139], v[138:139], v[42:43] op_sel_hi:[1,0]
	v_pk_mul_f32 v[206:207], v[206:207], v[42:43] op_sel_hi:[1,0]
	v_lshlrev_b32_e32 v18, 2, v62
	v_lshlrev_b32_e32 v18, 1, v58
	v_pk_mul_f32 v[14:15], v[14:15], v[42:43] op_sel_hi:[1,0]
	s_addc_u32 s25, s17, s27
	v_pk_mul_f32 v[6:7], v[6:7], v[96:97] op_sel_hi:[1,0]
	v_pk_mul_f32 v[12:13], v[12:13], v[96:97] op_sel_hi:[1,0]
	v_pk_mul_f32 v[2:3], v[2:3], v[96:97] op_sel_hi:[1,0]
	s_waitcnt vmcnt(2)
	v_pk_fma_f32 v[128:129], v[132:133], v[128:129], v[136:137]
	v_pk_fma_f32 v[34:35], v[130:131], v[34:35], v[134:135]
	v_pk_fma_f32 v[132:133], v[132:133], v[206:207], v[136:137]
	v_pk_fma_f32 v[130:131], v[130:131], v[138:139], v[134:135]
	v_cvt_pk_bf16_f32 v135, v132, v133
	v_cvt_pk_bf16_f32 v134, v130, v131
	v_lshl_add_u64 v[136:137], v[64:65], 0, s[26:27]
	s_waitcnt vmcnt(2)
	v_pk_fma_f32 v[32:33], v[158:159], v[32:33], v[162:163]
	v_pk_fma_f32 v[36:37], v[156:157], v[36:37], v[160:161]
	global_store_dwordx2 v[136:137], v[134:135], off
	v_cvt_pk_bf16_f32 v134, v36, v37
	v_cvt_pk_bf16_f32 v135, v32, v33
	global_store_dwordx2 v18, v[134:135], s[8:9]
	v_pk_mul_f32 v[134:135], v[204:205], v[42:43] op_sel_hi:[1,0]
	v_pk_fma_f32 v[14:15], v[156:157], v[14:15], v[160:161]
	v_pk_fma_f32 v[134:135], v[158:159], v[134:135], v[162:163]
	v_cvt_pk_bf16_f32 v136, v14, v15
	v_cvt_pk_bf16_f32 v137, v134, v135
	global_store_dwordx2 v18, v[136:137], s[24:25]
	v_lshlrev_b32_e32 v18, 1, v60
	v_pk_mul_f32 v[4:5], v[4:5], v[96:97] op_sel_hi:[1,0]
	v_cvt_pk_bf16_f32 v208, v34, v35
	v_cvt_pk_bf16_f32 v209, v128, v129
	global_store_dwordx2 v[210:211], v[208:209], off
	v_mov_b32_e32 v20, v25
	v_pk_mul_f32 v[20:21], v[20:21], v[96:97] op_sel_hi:[1,0]
	s_waitcnt vmcnt(5)
	v_pk_fma_f32 v[12:13], v[126:127], v[12:13], v[166:167]
	v_pk_fma_f32 v[136:137], v[124:125], v[6:7], v[164:165]
	v_cvt_pk_bf16_f32 v7, v12, v13
	v_cvt_pk_bf16_f32 v6, v136, v137
	global_store_dwordx2 v18, v[6:7], s[8:9]
	v_pk_mul_f32 v[6:7], v[16:17], v[42:43] op_sel_hi:[1,0]
	v_pk_mul_f32 v[16:17], v[30:31], v[42:43] op_sel_hi:[1,0]
	v_pk_fma_f32 v[30:31], v[124:125], v[6:7], v[164:165]
	v_pk_fma_f32 v[16:17], v[126:127], v[16:17], v[166:167]
	v_cvt_pk_bf16_f32 v6, v30, v31
	v_cvt_pk_bf16_f32 v7, v16, v17
	s_waitcnt vmcnt(6)
	v_pk_fma_f32 v[138:139], v[4:5], v[170:171], v[174:175]
	v_pk_fma_f32 v[212:213], v[2:3], v[168:169], v[172:173]
	global_store_dwordx2 v18, v[6:7], s[24:25]
	v_cvt_pk_bf16_f32 v2, v212, v213
	v_cvt_pk_bf16_f32 v3, v138, v139
	v_lshlrev_b32_e32 v6, 1, v62
	global_store_dwordx2 v6, v[2:3], s[8:9]
	v_pk_mul_f32 v[2:3], v[8:9], v[42:43] op_sel_hi:[1,0]
	v_pk_mul_f32 v[4:5], v[10:11], v[42:43] op_sel_hi:[1,0]
	v_pk_fma_f32 v[222:223], v[168:169], v[2:3], v[172:173]
	v_pk_fma_f32 v[220:221], v[170:171], v[4:5], v[174:175]
	v_cvt_pk_bf16_f32 v2, v222, v223
	v_cvt_pk_bf16_f32 v3, v220, v221
	global_store_dwordx2 v6, v[2:3], s[24:25]
	v_lshlrev_b32_e32 v2, 2, v66
	global_load_dwordx4 v[156:159], v2, s[28:29]
	global_load_dwordx4 v[160:163], v[68:69], off
	global_load_dwordx4 v[164:167], v[70:71], off
	global_load_dwordx4 v[168:171], v2, s[22:23]
	v_lshlrev_b32_e32 v10, 2, v72
	global_load_dwordx4 v[172:175], v10, s[28:29]
	global_load_dwordx4 v[204:207], v[74:75], off
	global_load_dwordx4 v[208:211], v[76:77], off
	v_lshlrev_b32_e32 v18, 2, v78
	global_load_dwordx4 v[216:219], v10, s[22:23]
	v_lshlrev_b32_e32 v92, 1, v66
	v_mov_b32_e32 v114, v119
	v_mov_b32_e32 v112, v117
	v_pk_mul_f32 v[26:27], v[26:27], v[96:97] op_sel_hi:[1,0]
	v_pk_mul_f32 v[28:29], v[28:29], v[96:97] op_sel_hi:[1,0]
	v_pk_mul_f32 v[94:95], v[94:95], v[96:97] op_sel_hi:[1,0]
	v_pk_mul_f32 v[108:109], v[108:109], v[42:43] op_sel_hi:[1,0]
	s_waitcnt vmcnt(16)
	v_pk_add_f32 v[6:7], v[40:41], 1.0 op_sel_hi:[1,0]
	v_pk_add_f32 v[8:9], v[38:39], 1.0 op_sel_hi:[1,0]
	s_waitcnt vmcnt(16)
	v_pk_fma_f32 v[4:5], v[6:7], v[128:129], v[178:179]
	v_pk_fma_f32 v[2:3], v[8:9], v[34:35], v[176:177]
	v_pk_fma_f32 v[126:127], v[6:7], v[132:133], v[178:179]
	v_pk_fma_f32 v[130:131], v[8:9], v[130:131], v[176:177]
	v_add_u32_e32 v6, 0x2008, v145
	s_waitcnt vmcnt(16)
	v_pk_add_f32 v[34:35], v[180:181], 1.0 op_sel_hi:[1,0]
	global_load_dwordx4 v[176:179], v18, s[28:29]
	v_pk_add_f32 v[10:11], v[182:183], 1.0 op_sel_hi:[1,0]
	ds_write2_b64 v6, v[130:131], v[126:127] offset1:1
	s_waitcnt vmcnt(17)
	v_pk_fma_f32 v[8:9], v[10:11], v[32:33], v[186:187]
	v_pk_fma_f32 v[6:7], v[34:35], v[36:37], v[184:185]
	v_pk_fma_f32 v[124:125], v[10:11], v[134:135], v[186:187]
	v_pk_fma_f32 v[128:129], v[34:35], v[14:15], v[184:185]
	v_add_u32_e32 v10, 0x2408, v145
	s_waitcnt vmcnt(17)
	v_pk_add_f32 v[14:15], v[190:191], 1.0 op_sel_hi:[1,0]
	v_pk_add_f32 v[32:33], v[188:189], 1.0 op_sel_hi:[1,0]
	ds_write_b128 v145, v[2:5]
	ds_write_b128 v145, v[6:9] offset:1024
	ds_write2_b64 v10, v[128:129], v[124:125] offset1:1
	s_waitcnt vmcnt(17)
	v_pk_fma_f32 v[12:13], v[14:15], v[12:13], v[194:195]
	v_pk_fma_f32 v[10:11], v[32:33], v[136:137], v[192:193]
	v_pk_fma_f32 v[132:133], v[14:15], v[16:17], v[194:195]
	v_pk_fma_f32 v[134:135], v[32:33], v[30:31], v[192:193]
	v_add_u32_e32 v14, 0x2808, v145
	global_load_dwordx4 v[180:183], v[80:81], off
	global_load_dwordx4 v[184:187], v[82:83], off
	ds_write_b128 v145, v[10:13] offset:2048
	v_lshlrev_b32_e32 v15, 2, v84
	ds_write2_b64 v14, v[134:135], v[132:133] offset1:1
	global_load_dwordx4 v[188:191], v18, s[22:23]
	global_load_dwordx4 v[192:195], v15, s[28:29]
	global_load_dwordx4 v[34:37], v[86:87], off
	global_load_dwordx4 v[38:41], v[88:89], off
	global_load_dwordx4 v[30:33], v15, s[22:23]
	s_waitcnt vmcnt(24)
	v_pk_add_f32 v[136:137], v[198:199], 1.0 op_sel_hi:[1,0]
	v_pk_add_f32 v[196:197], v[196:197], 1.0 op_sel_hi:[1,0]
	s_waitcnt vmcnt(24)
	v_pk_fma_f32 v[16:17], v[138:139], v[136:137], v[202:203]
	v_pk_fma_f32 v[136:137], v[136:137], v[220:221], v[202:203]
	v_pk_fma_f32 v[138:139], v[196:197], v[222:223], v[200:201]
	v_add_u32_e32 v18, 0x2c08, v145
	ds_write2_b64 v18, v[138:139], v[136:137] offset1:1
	v_mov_b32_e32 v18, v23
	v_pk_mul_f32 v[18:19], v[18:19], v[96:97] op_sel_hi:[1,0]
	v_pk_fma_f32 v[14:15], v[212:213], v[196:197], v[200:201]
	v_max_f32_e64 v102, |v16|, |v17|
	v_max3_f32 v102, |v14|, |v15|, v102
	v_pk_mul_f32 v[104:105], v[104:105], v[42:43] op_sel_hi:[1,0]
	ds_write_b128 v145, v[14:17] offset:3072
	s_waitcnt vmcnt(15)
	v_pk_add_f32 v[158:159], v[158:159], 1.0 op_sel_hi:[1,0]
	v_pk_add_f32 v[156:157], v[156:157], 1.0 op_sel_hi:[1,0]
	s_waitcnt vmcnt(13)
	v_pk_fma_f32 v[18:19], v[18:19], v[162:163], v[166:167]
	v_pk_fma_f32 v[20:21], v[20:21], v[160:161], v[164:165]
	v_cvt_pk_bf16_f32 v23, v18, v19
	v_cvt_pk_bf16_f32 v22, v20, v21
	global_store_dwordx2 v92, v[22:23], s[8:9]
	s_waitcnt vmcnt(13)
	v_pk_fma_f32 v[24:25], v[18:19], v[158:159], v[170:171]
	v_pk_fma_f32 v[22:23], v[20:21], v[156:157], v[168:169]
	v_pk_mul_f32 v[18:19], v[114:115], v[42:43] op_sel_hi:[1,0]
	v_pk_mul_f32 v[20:21], v[112:113], v[42:43] op_sel_hi:[1,0]
	v_pk_fma_f32 v[18:19], v[18:19], v[160:161], v[164:165]
	v_pk_fma_f32 v[20:21], v[20:21], v[162:163], v[166:167]
	v_cvt_pk_bf16_f32 v112, v18, v19
	v_cvt_pk_bf16_f32 v113, v20, v21
	global_store_dwordx2 v92, v[112:113], s[24:25]
	v_pk_fma_f32 v[112:113], v[20:21], v[158:159], v[170:171]
	v_pk_fma_f32 v[114:115], v[18:19], v[156:157], v[168:169]
	v_add_u32_e32 v18, 0x3008, v145
	ds_write2_b64 v18, v[114:115], v[112:113] offset1:1
	v_pk_mul_f32 v[18:19], v[98:99], v[96:97] op_sel_hi:[1,0]
	v_pk_mul_f32 v[20:21], v[110:111], v[96:97] op_sel_hi:[1,0]
	s_waitcnt vmcnt(11)
	v_pk_fma_f32 v[18:19], v[18:19], v[204:205], v[208:209]
	v_pk_fma_f32 v[20:21], v[20:21], v[206:207], v[210:211]
	v_cvt_pk_bf16_f32 v98, v18, v19
	v_cvt_pk_bf16_f32 v99, v20, v21
	v_lshlrev_b32_e32 v92, 1, v72
	global_store_dwordx2 v92, v[98:99], s[8:9]
	v_pk_mul_f32 v[98:99], v[120:121], v[42:43] op_sel_hi:[1,0]
	v_pk_mul_f32 v[110:111], v[122:123], v[42:43] op_sel_hi:[1,0]
	v_pk_fma_f32 v[120:121], v[98:99], v[204:205], v[208:209]
	v_pk_fma_f32 v[110:111], v[110:111], v[206:207], v[210:211]
	v_pk_add_f32 v[116:117], v[174:175], 1.0 op_sel_hi:[1,0]
	v_pk_add_f32 v[118:119], v[172:173], 1.0 op_sel_hi:[1,0]
	v_cvt_pk_bf16_f32 v98, v120, v121
	v_cvt_pk_bf16_f32 v99, v110, v111
	global_store_dwordx2 v92, v[98:99], s[24:25]
	s_waitcnt vmcnt(12)
	v_pk_fma_f32 v[98:99], v[110:111], v[116:117], v[218:219]
	v_pk_fma_f32 v[110:111], v[120:121], v[118:119], v[216:217]
	v_add_u32_e32 v92, 0x3408, v145
	ds_write2_b64 v92, v[110:111], v[98:99] offset1:1
	v_mov_b32_e32 v92, v97
	v_pk_mul_f32 v[92:93], v[92:93], v[96:97] op_sel_hi:[1,0]
	s_waitcnt vmcnt(9)
	v_pk_fma_f32 v[28:29], v[28:29], v[182:183], v[186:187]
	v_pk_fma_f32 v[26:27], v[26:27], v[180:181], v[184:185]
	v_pk_fma_f32 v[20:21], v[20:21], v[116:117], v[218:219]
	v_cvt_pk_bf16_f32 v120, v26, v27
	s_waitcnt vmcnt(5)
	v_pk_fma_f32 v[156:157], v[92:93], v[36:37], v[40:41]
	v_max_f32_e64 v92, |v4|, |v5|
	v_max_f32_e64 v93, |v8|, |v9|
	v_max3_f32 v92, |v2|, |v3|, v92
	v_max3_f32 v93, |v6|, |v7|, v93
	v_max3_f32 v92, v92, 0, v93
	v_max_f32_e64 v93, |v12|, |v13|
	v_cvt_pk_bf16_f32 v121, v28, v29
	v_max3_f32 v93, |v10|, |v11|, v93
	v_pk_fma_f32 v[18:19], v[18:19], v[118:119], v[216:217]
	v_pk_add_f32 v[116:117], v[178:179], 1.0 op_sel_hi:[1,0]
	global_store_dwordx2 v100, v[120:121], s[8:9]
	v_pk_add_f32 v[120:121], v[194:195], 1.0 op_sel_hi:[1,0]
	v_max3_f32 v92, v92, v93, v102
	v_max_f32_e64 v93, |v24|, |v25|
	v_max_f32_e64 v102, |v20|, |v21|
	v_pk_add_f32 v[118:119], v[176:177], 1.0 op_sel_hi:[1,0]
	v_pk_fma_f32 v[28:29], v[28:29], v[116:117], v[190:191]
	v_pk_add_f32 v[122:123], v[192:193], 1.0 op_sel_hi:[1,0]
	v_pk_fma_f32 v[158:159], v[94:95], v[34:35], v[38:39]
	s_waitcnt vmcnt(5)
	v_pk_fma_f32 v[96:97], v[156:157], v[120:121], v[32:33]
	v_max3_f32 v93, |v22|, |v23|, v93
	v_max3_f32 v102, |v18|, |v19|, v102
	v_pk_fma_f32 v[26:27], v[26:27], v[118:119], v[188:189]
	v_pk_fma_f32 v[94:95], v[158:159], v[122:123], v[30:31]
	v_max3_f32 v92, v92, v93, v102
	v_max_f32_e64 v93, |v28|, |v29|
	v_max_f32_e64 v102, |v96|, |v97|
	v_max3_f32 v93, |v26|, |v27|, v93
	v_max3_f32 v102, |v94|, |v95|, v102
	v_max3_f32 v102, v92, v93, v102
	ds_bpermute_b32 v160, v1, v102
	v_pk_mul_f32 v[92:93], v[106:107], v[42:43] op_sel_hi:[1,0]
	v_pk_fma_f32 v[106:107], v[108:109], v[180:181], v[184:185]
	v_pk_fma_f32 v[92:93], v[92:93], v[182:183], v[186:187]
	v_cvt_pk_bf16_f32 v108, v106, v107
	s_waitcnt lgkmcnt(0)
	v_max_f32_e32 v109, v160, v160
	v_max_f32_e32 v102, v102, v109
	ds_bpermute_b32 v160, v49, v102
	v_cvt_pk_bf16_f32 v109, v92, v93
	global_store_dwordx2 v100, v[108:109], s[24:25]
	v_pk_fma_f32 v[92:93], v[92:93], v[116:117], v[190:191]
	v_pk_fma_f32 v[116:117], v[106:107], v[118:119], v[188:189]
	s_waitcnt lgkmcnt(0)
	v_max_f32_e32 v100, v160, v160
	v_max_f32_e32 v100, v102, v100
	ds_bpermute_b32 v102, v59, v100
	v_add_u32_e32 v106, 0x3808, v145
	ds_write2_b64 v106, v[116:117], v[92:93] offset1:1
	v_cvt_pk_bf16_f32 v106, v158, v159
	v_cvt_pk_bf16_f32 v107, v156, v157
	s_waitcnt lgkmcnt(1)
	v_max_f32_e32 v102, v102, v102
	v_max_f32_e32 v100, v100, v102
	ds_bpermute_b32 v102, v61, v100
	v_lshlrev_b32_e32 v108, 1, v84
	global_store_dwordx2 v108, v[106:107], s[8:9]
	v_pk_fma_f32 v[34:35], v[104:105], v[34:35], v[38:39]
	ds_write_b128 v145, v[22:25] offset:4096
	s_waitcnt lgkmcnt(1)
	v_max_f32_e32 v102, v102, v102
	v_max_f32_e32 v102, v100, v102
	ds_bpermute_b32 v106, v63, v102
	v_mov_b32_e32 v100, v103
	v_pk_mul_f32 v[100:101], v[100:101], v[42:43] op_sel_hi:[1,0]
	ds_write_b128 v145, v[18:21] offset:5120
	v_pk_fma_f32 v[36:37], v[100:101], v[36:37], v[40:41]
	s_waitcnt lgkmcnt(1)
	v_max_f32_e32 v38, v106, v106
	v_max_f32_e32 v40, v102, v38
	ds_bpermute_b32 v41, v67, v40
	v_pk_fma_f32 v[118:119], v[36:37], v[120:121], v[32:33]
	v_cvt_pk_bf16_f32 v39, v36, v37
	v_pk_fma_f32 v[120:121], v[34:35], v[122:123], v[30:31]
	v_add_u32_e32 v30, 0x3c08, v145
	s_waitcnt lgkmcnt(0)
	v_max3_f32 v32, v40, v41, s37
	v_div_scale_f32 v33, s[8:9], v32, v32, s38
	v_rcp_f32_e32 v36, v33
	ds_write2_b64 v30, v[120:121], v[118:119] offset1:1
	v_cvt_pk_bf16_f32 v38, v34, v35
	global_store_dwordx2 v108, v[38:39], s[24:25]
	v_fma_f32 v30, -v33, v36, 1.0
	v_fmac_f32_e32 v36, v30, v36
	v_div_scale_f32 v30, vcc, s38, v32, s38
	v_mul_f32_e32 v31, v30, v36
	v_fma_f32 v34, -v33, v31, v30
	v_fmac_f32_e32 v31, v34, v36
	v_fma_f32 v30, -v33, v31, v30
	v_div_fmas_f32 v30, v30, v36, v31
	v_div_fixup_f32 v108, v30, v32, s38
	v_fmaak_f32 v2, v2, v108, 0x4b400000
	v_med3_f32 v30, v2, s39, v153
	v_fmaak_f32 v2, v3, v108, 0x4b400000
	v_med3_f32 v31, v2, s39, v153
	v_fmaak_f32 v2, v4, v108, 0x4b400000
	v_fmaak_f32 v3, v5, v108, 0x4b400000
	v_med3_f32 v2, v2, s39, v153
	v_med3_f32 v3, v3, s39, v153
	v_perm_b32 v33, v3, v2, s40
	v_fmaak_f32 v2, v6, v108, 0x4b400000
	v_med3_f32 v34, v2, s39, v153
	v_fmaak_f32 v2, v7, v108, 0x4b400000
	v_med3_f32 v35, v2, s39, v153
	v_fmaak_f32 v2, v8, v108, 0x4b400000
	v_fmaak_f32 v3, v9, v108, 0x4b400000
	v_med3_f32 v2, v2, s39, v153
	v_med3_f32 v3, v3, s39, v153
	v_perm_b32 v36, v3, v2, s40
	v_fmaak_f32 v2, v10, v108, 0x4b400000
	v_med3_f32 v37, v2, s39, v153
	v_fmaak_f32 v2, v11, v108, 0x4b400000
	v_med3_f32 v38, v2, s39, v153
	v_fmaak_f32 v2, v12, v108, 0x4b400000
	v_fmaak_f32 v3, v13, v108, 0x4b400000
	v_med3_f32 v2, v2, s39, v153
	v_med3_f32 v3, v3, s39, v153
	v_perm_b32 v39, v3, v2, s40
	v_fmaak_f32 v2, v14, v108, 0x4b400000
	v_med3_f32 v40, v2, s39, v153
	v_fmaak_f32 v2, v15, v108, 0x4b400000
	v_med3_f32 v41, v2, s39, v153
	v_fmaak_f32 v2, v16, v108, 0x4b400000
	v_fmaak_f32 v3, v17, v108, 0x4b400000
	v_med3_f32 v2, v2, s39, v153
	v_med3_f32 v3, v3, s39, v153
	v_perm_b32 v42, v3, v2, s40
	v_fmaak_f32 v2, v22, v108, 0x4b400000
	v_med3_f32 v22, v2, s39, v153
	v_fmaak_f32 v2, v23, v108, 0x4b400000
	v_med3_f32 v23, v2, s39, v153
	v_fmaak_f32 v2, v24, v108, 0x4b400000
	v_fmaak_f32 v3, v25, v108, 0x4b400000
	v_med3_f32 v2, v2, s39, v153
	v_med3_f32 v3, v3, s39, v153
	v_perm_b32 v24, v3, v2, s40
	v_max_f32_e64 v2, |v126|, |v127|
	v_max_f32_e64 v3, |v124|, |v125|
	v_max3_f32 v2, |v130|, |v131|, v2
	v_max3_f32 v3, |v128|, |v129|, v3
	v_max3_f32 v2, v2, 0, v3
	v_max_f32_e64 v3, |v132|, |v133|
	v_max_f32_e64 v4, |v136|, |v137|
	v_max3_f32 v3, |v134|, |v135|, v3
	v_max3_f32 v4, |v138|, |v139|, v4
	v_max3_f32 v2, v2, v3, v4
	v_max_f32_e64 v3, |v112|, |v113|
	v_max_f32_e64 v4, |v98|, |v99|
	v_max3_f32 v3, |v114|, |v115|, v3
	v_max3_f32 v4, |v110|, |v111|, v4
	v_max3_f32 v2, v2, v3, v4
	v_max_f32_e64 v3, |v92|, |v93|
	v_max_f32_e64 v4, |v118|, |v119|
	v_max3_f32 v3, |v116|, |v117|, v3
	v_max3_f32 v4, |v120|, |v121|, v4
	v_max3_f32 v2, v2, v3, v4
	ds_bpermute_b32 v3, v1, v2
	v_fmaak_f32 v4, v18, v108, 0x4b400000
	v_med3_f32 v100, v4, s39, v153
	v_fmaak_f32 v4, v19, v108, 0x4b400000
	v_med3_f32 v101, v4, s39, v153
	s_waitcnt lgkmcnt(0)
	v_max_f32_e32 v3, v3, v3
	v_max_f32_e32 v2, v2, v3
	ds_bpermute_b32 v3, v49, v2
	v_fmaak_f32 v4, v20, v108, 0x4b400000
	v_fmaak_f32 v5, v21, v108, 0x4b400000
	v_med3_f32 v4, v4, s39, v153
	v_med3_f32 v5, v5, s39, v153
	s_waitcnt lgkmcnt(0)
	v_max_f32_e32 v3, v3, v3
	v_max_f32_e32 v2, v2, v3
	ds_bpermute_b32 v3, v59, v2
	v_perm_b32 v102, v5, v4, s40
	v_fmaak_f32 v4, v26, v108, 0x4b400000
	v_med3_f32 v103, v4, s39, v153
	v_fmaak_f32 v4, v27, v108, 0x4b400000
	s_waitcnt lgkmcnt(0)
	v_max_f32_e32 v3, v3, v3
	v_max_f32_e32 v2, v2, v3
	ds_bpermute_b32 v3, v61, v2
	v_med3_f32 v104, v4, s39, v153
	v_fmaak_f32 v4, v28, v108, 0x4b400000
	v_fmaak_f32 v5, v29, v108, 0x4b400000
	v_med3_f32 v4, v4, s39, v153
	s_waitcnt lgkmcnt(0)
	v_max_f32_e32 v3, v3, v3
	v_max_f32_e32 v2, v2, v3
	ds_bpermute_b32 v3, v63, v2
	v_med3_f32 v5, v5, s39, v153
	v_perm_b32 v106, v5, v4, s40
	v_fmaak_f32 v4, v94, v108, 0x4b400000
	v_med3_f32 v105, v4, s39, v153
	s_waitcnt lgkmcnt(0)
	v_max_f32_e32 v3, v3, v3
	v_max_f32_e32 v2, v2, v3
	ds_bpermute_b32 v3, v67, v2
	v_fmaak_f32 v4, v95, v108, 0x4b400000
	v_med3_f32 v107, v4, s39, v153
	v_fmaak_f32 v4, v96, v108, 0x4b400000
	v_fmaak_f32 v5, v97, v108, 0x4b400000
	s_waitcnt lgkmcnt(0)
	v_max3_f32 v10, v2, v3, s37
	v_div_scale_f32 v2, s[8:9], v10, v10, s38
	v_rcp_f32_e32 v3, v2
	v_med3_f32 v4, v4, s39, v153
	v_med3_f32 v5, v5, s39, v153
	v_perm_b32 v108, v5, v4, s40
	v_fma_f32 v4, -v2, v3, 1.0
	v_fmac_f32_e32 v3, v4, v3
	v_div_scale_f32 v4, vcc, s38, v10, s38
	v_mul_f32_e32 v5, v4, v3
	v_fma_f32 v6, -v2, v5, v4
	v_fmac_f32_e32 v5, v6, v3
	v_fma_f32 v2, -v2, v5, v4
	v_div_fmas_f32 v2, v2, v3, v5
	v_div_fixup_f32 v2, v2, v10, s38
	v_fmaak_f32 v3, v130, v2, 0x4b400000
	v_med3_f32 v11, v3, s39, v153
	v_fmaak_f32 v3, v131, v2, 0x4b400000
	v_med3_f32 v12, v3, s39, v153
	v_fmaak_f32 v3, v126, v2, 0x4b400000
	v_fmaak_f32 v4, v127, v2, 0x4b400000
	v_med3_f32 v3, v3, s39, v153
	v_med3_f32 v4, v4, s39, v153
	v_perm_b32 v13, v4, v3, s40
	v_fmaak_f32 v3, v128, v2, 0x4b400000
	v_med3_f32 v14, v3, s39, v153
	v_fmaak_f32 v3, v129, v2, 0x4b400000
	v_med3_f32 v15, v3, s39, v153
	v_fmaak_f32 v3, v124, v2, 0x4b400000
	v_fmaak_f32 v4, v125, v2, 0x4b400000
	v_med3_f32 v3, v3, s39, v153
	v_med3_f32 v4, v4, s39, v153
	v_perm_b32 v16, v4, v3, s40
	v_fmaak_f32 v3, v134, v2, 0x4b400000
	v_med3_f32 v17, v3, s39, v153
	v_fmaak_f32 v3, v135, v2, 0x4b400000
	v_med3_f32 v18, v3, s39, v153
	v_fmaak_f32 v3, v132, v2, 0x4b400000
	v_fmaak_f32 v4, v133, v2, 0x4b400000
	v_med3_f32 v3, v3, s39, v153
	v_med3_f32 v4, v4, s39, v153
	v_perm_b32 v19, v4, v3, s40
	v_fmaak_f32 v3, v138, v2, 0x4b400000
	v_med3_f32 v20, v3, s39, v153
	v_fmaak_f32 v3, v139, v2, 0x4b400000
	v_med3_f32 v21, v3, s39, v153
	v_fmaak_f32 v3, v136, v2, 0x4b400000
	v_fmaak_f32 v4, v137, v2, 0x4b400000
	v_med3_f32 v3, v3, s39, v153
	v_med3_f32 v4, v4, s39, v153
	v_perm_b32 v25, v4, v3, s40
	v_fmaak_f32 v3, v114, v2, 0x4b400000
	ds_write_b128 v145, v[26:29] offset:6144
	v_med3_f32 v26, v3, s39, v153
	v_fmaak_f32 v3, v115, v2, 0x4b400000
	v_med3_f32 v27, v3, s39, v153
	v_fmaak_f32 v3, v112, v2, 0x4b400000
	v_fmaak_f32 v4, v113, v2, 0x4b400000
	v_med3_f32 v3, v3, s39, v153
	v_med3_f32 v4, v4, s39, v153
	v_perm_b32 v28, v4, v3, s40
	v_fmaak_f32 v3, v110, v2, 0x4b400000
	v_med3_f32 v29, v3, s39, v153
	v_fmaak_f32 v3, v111, v2, 0x4b400000
	ds_write_b128 v145, v[94:97] offset:7168
	v_med3_f32 v94, v3, s39, v153
	v_fmaak_f32 v3, v98, v2, 0x4b400000
	v_fmaak_f32 v4, v99, v2, 0x4b400000
	v_med3_f32 v3, v3, s39, v153
	v_med3_f32 v4, v4, s39, v153
	v_perm_b32 v95, v4, v3, s40
	v_fmaak_f32 v3, v116, v2, 0x4b400000
	v_med3_f32 v96, v3, s39, v153
	v_fmaak_f32 v3, v117, v2, 0x4b400000
	v_med3_f32 v97, v3, s39, v153
	v_fmaak_f32 v3, v92, v2, 0x4b400000
	v_fmaak_f32 v4, v93, v2, 0x4b400000
	v_med3_f32 v3, v3, s39, v153
	v_med3_f32 v4, v4, s39, v153
	v_perm_b32 v98, v4, v3, s40
	v_fmaak_f32 v3, v120, v2, 0x4b400000
	v_med3_f32 v92, v3, s39, v153
	v_fmaak_f32 v3, v121, v2, 0x4b400000
	v_med3_f32 v93, v3, s39, v153
	v_fmaak_f32 v3, v118, v2, 0x4b400000
	v_fmaak_f32 v2, v119, v2, 0x4b400000
	v_med3_f32 v3, v3, s39, v153
	v_med3_f32 v2, v2, s39, v153
	v_perm_b32 v99, v2, v3, s40
	s_mov_b64 s[8:9], 0
	v_mov_b32_e32 v109, v73
	v_mov_b32_e32 v2, 0
	v_mov_b32_e32 v3, v43
	v_mov_b32_e32 v4, v43
	v_mov_b32_e32 v5, v43
	v_mov_b32_e32 v6, 0
	v_mov_b32_e32 v7, v43
	v_mov_b32_e32 v8, v43
	v_mov_b32_e32 v9, v43
	s_waitcnt lgkmcnt(0)
	s_barrier
